# LN1 row loop: two rows of loads in flight, no wait on the previous row's stores
# speedup vs baseline: 1.0001x; 1.0001x over previous
; #define LAS __attribute__((address_space(3)))
; __device__ __forceinline__ void ln1_row(const u32x4 ra, const u32x4 rb, const LAS float* cv  , bf16_t* __restrict__ hf, unsigned char* __restrict__ hf8, float* __restrict__ stats, int row, int lane) {
;     asm volatile("" : "+v"(cv));
;     const int c0 = lane * 16;
;     f32x4 v[4]; float s = 0.f;
;     unpack_t16r(ra, rb, v);
; #pragma unroll
;     for (int j = 0; j < 4; ++j) s += (v[j].x + v[j].y) + (v[j].z + v[j].w);
;     const float mean = wave_sum(s) * (1.f / D); float s2 = 0.f;
; #pragma unroll
;     for (int j = 0; j < 4; ++j) { v[j] = v[j] - mean; s2 += (v[j].x * v[j].x + v[j].y * v[j].y) + (v[j].z * v[j].z + v[j].w * v[j].w); }
;     const float rstd = 1.f / sqrtf(wave_sum(s2) * (1.f / D) + LN_EPS);
;     if (lane == 0) *(f32x2*)(stats + 2 * (size_t)row) = (f32x2){mean, rstd};
;     u32x4 ob[2], o8;
; #pragma unroll
;     for (int j = 0; j < 4; ++j) { const int col = c0 + 4 * j;
;         const f32x4 gg = *(const LAS f32x4*)(cv + col), bv = *(const LAS f32x4*)(cv + 1024 + col), sc1 = *(const LAS f32x4*)(cv + 2048 + col), sh = *(const LAS f32x4*)(cv + 3072 + col);
;         const f32x4 h4 = (v[j] * rstd * gg + bv) * sc1 + sh;
;         const unsigned p0 = pk2(h4.x, h4.y), p1 = pk2(h4.z, h4.w);
;         if (j == 0) { ob[0].x = p0; ob[0].y = p1; } else if (j == 1) { ob[0].z = p0; ob[0].w = p1; } else if (j == 2) { ob[1].x = p0; ob[1].y = p1; } else { ob[1].z = p0; ob[1].w = p1; }
;         const f32x4 h8 = h4 * S_HF8;
;         int w0 = __builtin_amdgcn_cvt_pk_fp8_f32(clamp8(h8.x), clamp8(h8.y), 0, false); w0 = __builtin_amdgcn_cvt_pk_fp8_f32(clamp8(h8.z), clamp8(h8.w), w0, true);
;         if (j == 0) o8.x = (unsigned)w0; else if (j == 1) o8.y = (unsigned)w0; else if (j == 2) o8.z = (unsigned)w0; else o8.w = (unsigned)w0; }
;     *(u32x4*)(hf + (size_t)row * D + c0) = ob[0]; *(u32x4*)(hf + (size_t)row * D + c0 + 8) = ob[1];
;     *(u32x4*)(hf8 + (size_t)row * D + c0) = o8;
; }
; __global__ void __launch_bounds__(NW * 64, 2) mk_fwd(Args args) {
;     ...
;             { const bf16_t* tp = (const bf16_t*)(ws + WS_TB) + (size_t)(c * 256 + wave * 32) * D + lane2 * 16;
;               u32x4 ra = *(const u32x4*)tp, rb = *(const u32x4*)(tp + 8);
; #pragma unroll 1
;               for (int i = 0; i < 32; ++i) {
;                   const u32x4 ca = ra, cb = rb; const int nx = i < 31 ? i + 1 : i;
.LBB0_414:
	s_or_b64 exec, exec, s[4:5]
	s_lshl_b32 s96, s2, 8
	v_readlane_b32 s4, v252, 42
	s_add_i32 s4, s96, s4
	s_ashr_i32 s5, s4, 31
	s_lshl_b64 s[4:5], s[4:5], 11
	v_lshlrev_b32_e32 v16, 4, v0
	s_add_u32 s4, s50, s4
	v_ashrrev_i32_e32 v17, 31, v16
	s_addc_u32 s5, s51, s5
	v_lshlrev_b64 v[2:3], 1, v[16:17]
	v_lshl_add_u64 v[18:19], s[4:5], 0, v[2:3]
	s_waitcnt lgkmcnt(0)
	s_barrier
	global_load_dwordx4 v[12:15], v[18:19], off offset:16
	global_load_dwordx4 v[8:11], v[18:19], off
	v_lshl_add_u64 v[20:21], s[48:49], 0, v[2:3]
	v_lshl_add_u64 v[22:23], s[58:59], 0, v[16:17]
	v_cmp_ne_u32_e64 s[10:11], 0, v0
	s_movk_i32 s8, 0x400
	s_mov_b32 s6, s1
	global_load_dwordx4 v[114:117], v[18:19], off offset:2064
	global_load_dwordx4 v[118:121], v[18:19], off offset:2048
	s_mov_b32 s99, 0
	s_waitcnt vmcnt(2)
	s_branch .LBB0_416
.LBB0_415:
	s_or_b64 exec, exec, s[4:5]
	v_mov_b32_e32 v110, v40
	v_mov_b32_e32 v111, v38
	v_mov_b32_e32 v113, v8
	v_lshl_add_u32 v8, v16, 2, v15
	v_mov_b32_e32 v38, v41
	v_pk_mul_f32 v[40:41], v[110:111], v[44:45] op_sel_hi:[1,0]
	ds_read_b128 v[46:49], v8
	ds_read_b128 v[50:53], v8 offset:16
	ds_read_b128 v[54:57], v8 offset:32
	ds_read_b128 v[58:61], v8 offset:48
	ds_read_b128 v[62:65], v8 offset:4096
	ds_read_b128 v[66:69], v8 offset:4112
	ds_read_b128 v[70:73], v8 offset:8192
	ds_read_b128 v[74:77], v8 offset:8208
	ds_read_b128 v[78:81], v8 offset:12288
	ds_read_b128 v[82:85], v8 offset:12304
	ds_read_b128 v[86:89], v8 offset:4128
	ds_read_b128 v[90:93], v8 offset:4144
	ds_read_b128 v[94:97], v8 offset:8224
	ds_read_b128 v[98:101], v8 offset:8240
	ds_read_b128 v[102:105], v8 offset:12320
	ds_read_b128 v[106:109], v8 offset:12336
	v_pk_mul_f32 v[38:39], v[38:39], v[44:45] op_sel_hi:[1,0]
	s_waitcnt lgkmcnt(11)
	v_pk_fma_f32 v[40:41], v[40:41], v[46:47], v[62:63]
	v_pk_fma_f32 v[38:39], v[38:39], v[48:49], v[64:65]
	s_waitcnt lgkmcnt(7)
	v_pk_fma_f32 v[40:41], v[40:41], v[70:71], v[78:79]
	v_mov_b32_e32 v13, v42
	v_pk_fma_f32 v[42:43], v[38:39], v[72:73], v[80:81]
	v_pk_mul_f32 v[38:39], v[40:41], s[88:89] op_sel_hi:[1,0]
	v_mov_b32_e32 v112, v36
	v_med3_f32 v8, v38, s27, v204
	v_med3_f32 v15, v39, s27, v204
	v_mov_b32_e32 v36, v24
	v_cvt_pk_fp8_f32 v36, v8, v15
	v_pk_mul_f32 v[38:39], v[42:43], s[88:89] op_sel_hi:[1,0]
	v_pk_mul_f32 v[32:33], v[32:33], v[44:45] op_sel_hi:[1,0]
	v_med3_f32 v8, v38, s27, v204
	v_med3_f32 v15, v39, s27, v204
	v_pk_mul_f32 v[38:39], v[112:113], v[44:45] op_sel_hi:[1,0]
	v_cvt_pk_fp8_f32 v36, v8, v15 op_sel:[0,0,1]
	v_pk_fma_f32 v[38:39], v[38:39], v[50:51], v[66:67]
	v_mov_b32_e32 v8, v37
	s_waitcnt lgkmcnt(6)
	v_pk_fma_f32 v[46:47], v[38:39], v[74:75], v[82:83]
	v_pk_mul_f32 v[8:9], v[8:9], v[44:45] op_sel_hi:[1,0]
	v_pk_mul_f32 v[38:39], v[46:47], s[88:89] op_sel_hi:[1,0]
	v_mov_b32_e32 v37, v24
	v_med3_f32 v15, v38, s27, v204
	v_med3_f32 v17, v39, s27, v204
	v_pk_fma_f32 v[8:9], v[8:9], v[52:53], v[68:69]
	v_cvt_pk_fp8_f32 v37, v15, v17
	v_pk_fma_f32 v[8:9], v[8:9], v[76:77], v[84:85]
	s_waitcnt lgkmcnt(5)
	v_pk_fma_f32 v[32:33], v[32:33], v[54:55], v[86:87]
	v_pk_mul_f32 v[38:39], v[8:9], s[88:89] op_sel_hi:[1,0]
	s_waitcnt lgkmcnt(1)
	v_pk_fma_f32 v[32:33], v[32:33], v[94:95], v[102:103]
	v_med3_f32 v15, v38, s27, v204
	v_med3_f32 v17, v39, s27, v204
	v_pk_mul_f32 v[38:39], v[32:33], s[88:89] op_sel_hi:[1,0]
	v_cvt_pk_fp8_f32 v37, v15, v17 op_sel:[0,0,1]
	v_pk_mul_f32 v[34:35], v[34:35], v[44:45] op_sel_hi:[1,0]
	v_med3_f32 v15, v38, s27, v204
	v_med3_f32 v17, v39, s27, v204
	v_mov_b32_e32 v38, v24
	v_pk_fma_f32 v[34:35], v[34:35], v[56:57], v[88:89]
	v_cvt_pk_fp8_f32 v38, v15, v17
	v_pk_fma_f32 v[34:35], v[34:35], v[96:97], v[104:105]
	v_pk_mul_f32 v[12:13], v[12:13], v[44:45] op_sel_hi:[1,0]
	v_pk_mul_f32 v[48:49], v[34:35], s[88:89] op_sel_hi:[1,0]
	v_pk_fma_f32 v[12:13], v[12:13], v[58:59], v[90:91]
	v_med3_f32 v15, v48, s27, v204
	v_med3_f32 v17, v49, s27, v204
	v_cvt_pk_fp8_f32 v38, v15, v17 op_sel:[0,0,1]
	v_mov_b32_e32 v15, v26
	v_pk_mul_f32 v[14:15], v[14:15], v[44:45] op_sel_hi:[1,0]
	v_mov_b32_e32 v39, v24
	v_pk_fma_f32 v[14:15], v[14:15], v[60:61], v[92:93]
	v_bfe_u32 v17, v34, 16, 1
	s_waitcnt lgkmcnt(0)
	v_pk_fma_f32 v[26:27], v[14:15], v[100:101], v[108:109]
	v_pk_fma_f32 v[14:15], v[12:13], v[98:99], v[106:107]
	v_add3_u32 v17, v34, v17, s28
	v_pk_mul_f32 v[12:13], v[14:15], s[88:89] op_sel_hi:[1,0]
	v_lshrrev_b32_e32 v17, 16, v17
	v_med3_f32 v12, v12, s27, v204
	v_med3_f32 v13, v13, s27, v204
	v_cvt_pk_fp8_f32 v39, v12, v13
	v_pk_mul_f32 v[12:13], v[26:27], s[88:89] op_sel_hi:[1,0]
	v_bfe_u32 v25, v40, 16, 1
	v_med3_f32 v12, v12, s27, v204
	v_med3_f32 v13, v13, s27, v204
	v_cvt_pk_fp8_f32 v39, v12, v13 op_sel:[0,0,1]
	v_bfe_u32 v13, v32, 16, 1
	v_bfe_u32 v12, v33, 16, 1
	v_add3_u32 v13, v32, v13, s28
	v_add3_u32 v12, v33, v12, s28
	v_lshrrev_b32_e32 v13, 16, v13
	v_and_or_b32 v12, v12, s26, v13
	v_bfe_u32 v13, v35, 16, 1
	v_add3_u32 v13, v35, v13, s28
	v_and_or_b32 v13, v13, s26, v17
	v_bfe_u32 v17, v15, 16, 1
	v_add3_u32 v15, v15, v17, s28
	v_bfe_u32 v17, v14, 16, 1
	v_add3_u32 v14, v14, v17, s28
	v_lshrrev_b32_e32 v14, 16, v14
	v_bfe_u32 v17, v26, 16, 1
	v_and_or_b32 v14, v15, s26, v14
	v_bfe_u32 v15, v27, 16, 1
	v_add3_u32 v17, v26, v17, s28
	v_add3_u32 v15, v27, v15, s28
	v_lshrrev_b32_e32 v17, 16, v17
	v_and_or_b32 v15, v15, s26, v17
	v_bfe_u32 v17, v41, 16, 1
	v_add3_u32 v25, v40, v25, s28
	v_add3_u32 v17, v41, v17, s28
	v_lshrrev_b32_e32 v25, 16, v25
	v_and_or_b32 v32, v17, s26, v25
	v_bfe_u32 v25, v42, 16, 1
	v_bfe_u32 v17, v43, 16, 1
	v_add3_u32 v25, v42, v25, s28
	v_add3_u32 v17, v43, v17, s28
	v_lshrrev_b32_e32 v25, 16, v25
	v_and_or_b32 v33, v17, s26, v25
	v_bfe_u32 v25, v46, 16, 1
	v_bfe_u32 v17, v47, 16, 1
	v_add3_u32 v25, v46, v25, s28
	v_add3_u32 v17, v47, v17, s28
	v_lshrrev_b32_e32 v25, 16, v25
	v_and_or_b32 v34, v17, s26, v25
	v_bfe_u32 v17, v9, 16, 1
	v_add3_u32 v9, v9, v17, s28
	v_bfe_u32 v17, v8, 16, 1
	v_add3_u32 v8, v8, v17, s28
	v_lshrrev_b32_e32 v8, 16, v8
	v_and_or_b32 v35, v9, s26, v8
	v_lshlrev_b64 v[8:9], 10, v[10:11]
	v_lshlrev_b64 v[10:11], 11, v[10:11]
	v_lshl_add_u64 v[10:11], v[20:21], 0, v[10:11]
	v_lshl_add_u64 v[8:9], v[22:23], 0, v[8:9]
	global_store_dwordx4 v[10:11], v[32:35], off
	global_store_dwordx4 v[10:11], v[12:15], off offset:16
	global_store_dwordx4 v[8:9], v[36:39], off
	s_addk_i32 s8, 0x400
	s_add_i32 s6, s6, 1
	s_waitcnt vmcnt(6)
	s_xor_b32 s99, s99, 1
	s_cbranch_scc0 .Lln1_cpA
	v_mov_b64_e32 v[10:11], v[120:121]
	v_mov_b64_e32 v[14:15], v[116:117]
	v_mov_b64_e32 v[8:9], v[118:119]
	v_mov_b64_e32 v[12:13], v[114:115]
	s_branch .Lln1_cp_done
; __device__ __forceinline__ void ln1_row(const u32x4 ra, const u32x4 rb, const LAS float* cv  , bf16_t* __restrict__ hf, unsigned char* __restrict__ hf8, float* __restrict__ stats, int row, int lane) {
;     ...
;     f32x4 v[4]; float s = 0.f;
;     unpack_t16r(ra, rb, v);
; #pragma unroll
;     for (int j = 0; j < 4; ++j) s += (v[j].x + v[j].y) + (v[j].z + v[j].w);
;     const float mean = wave_sum(s) * (1.f / D); float s2 = 0.f;
; #pragma unroll
;     for (int j = 0; j < 4; ++j) { v[j] = v[j] - mean; s2 += (v[j].x * v[j].x + v[j].y * v[j].y) + (v[j].z * v[j].z + v[j].w * v[j].w); }
;     const float rstd = 1.f / sqrtf(wave_sum(s2) * (1.f / D) + LN_EPS);
;     if (lane == 0) *(f32x2*)(stats + 2 * (size_t)row) = (f32x2){mean, rstd};
; __global__ void __launch_bounds__(NW * 64, 2) mk_fwd(Args args) {
;     ...
;               for (int i = 0; i < 32; ++i) {
;                   const u32x4 ca = ra, cb = rb; const int nx = i < 31 ? i + 1 : i;
;                   ra = *(const u32x4*)(tp + (size_t)nx * D); rb = *(const u32x4*)(tp + (size_t)nx * D + 8);
.Lln1_cpA:
	v_mov_b64_e32 v[10:11], v[6:7]
	v_mov_b64_e32 v[14:15], v[2:3]
	v_mov_b64_e32 v[8:9], v[4:5]
	v_mov_b64_e32 v[12:13], v[0:1]
.Lln1_cp_done:
	s_cmpk_eq_u32 s8, 0x8400
	s_cbranch_scc1 .LBB0_420
.LBB0_416:
	s_add_i32 s16, s8, 0x400
	s_min_u32 s16, s16, 0x7c00
	v_lshl_add_u64 v[122:123], s[16:17], 1, v[18:19]
	s_cmp_eq_u32 s99, 0
	s_cbranch_scc0 .Lln1_ldB
	global_load_dwordx4 v[0:3], v[122:123], off offset:16
	global_load_dwordx4 v[4:7], v[122:123], off
	s_branch .Lln1_ld_done
.Lln1_ldB:
	global_load_dwordx4 v[114:117], v[122:123], off offset:16
	global_load_dwordx4 v[118:121], v[122:123], off
.Lln1_ld_done:
	v_lshlrev_b32_e32 v41, 16, v9
	v_lshlrev_b32_e32 v40, 16, v8
	v_and_b32_e32 v39, 0xffff0000, v9
	v_and_b32_e32 v38, 0xffff0000, v8
	v_pk_add_f32 v[8:9], v[40:41], v[38:39]
	v_lshlrev_b32_e32 v37, 16, v11
	v_add_f32_e32 v8, v8, v9
	v_add_f32_e32 v27, 0, v8
	v_lshlrev_b32_e32 v36, 16, v10
	v_and_b32_e32 v9, 0xffff0000, v11
	v_and_b32_e32 v8, 0xffff0000, v10
	v_pk_add_f32 v[10:11], v[36:37], v[8:9]
	v_lshlrev_b32_e32 v32, 16, v12
	v_and_b32_e32 v33, 0xffff0000, v12
	v_lshlrev_b32_e32 v34, 16, v13
	v_and_b32_e32 v35, 0xffff0000, v13
	v_pk_add_f32 v[10:11], v[10:11], v[10:11] op_sel_hi:[0,1]
	v_lshlrev_b32_e32 v12, 16, v14
	v_and_b32_e32 v42, 0xffff0000, v14
	v_lshlrev_b32_e32 v14, 16, v15
	v_and_b32_e32 v26, 0xffff0000, v15
	v_add_f32_e32 v13, v32, v33
	v_add_f32_e32 v43, v34, v35
	v_mov_b32_e32 v15, v11
	v_pk_add_f32 v[44:45], v[12:13], v[42:43]
	v_pk_add_f32 v[10:11], v[14:15], v[26:27]
	s_nop 0
	v_pk_add_f32 v[10:11], v[44:45], v[10:11]
	s_nop 0
	v_add_f32_e32 v10, v10, v11
	s_nop 1
	v_add_f32_dpp v10, v10, v10 quad_perm:[1,0,3,2] row_mask:0xf bank_mask:0xf bound_ctrl:1
	s_nop 1
	v_add_f32_dpp v10, v10, v10 quad_perm:[2,3,0,1] row_mask:0xf bank_mask:0xf bound_ctrl:1
	s_nop 1
	v_add_f32_dpp v10, v10, v10 row_half_mirror row_mask:0xf bank_mask:0xf bound_ctrl:1
	s_nop 1
	v_add_f32_dpp v10, v10, v10 row_mirror row_mask:0xf bank_mask:0xf bound_ctrl:1
	s_nop 0
	v_readlane_b32 s7, v10, 16
	v_readlane_b32 s9, v10, 48
	v_readlane_b32 s4, v10, 0
	v_readlane_b32 s5, v10, 32
	v_mov_b32_e32 v10, s7
	v_mov_b32_e32 v11, s9
	v_pk_add_f32 v[10:11], s[4:5], v[10:11]
	s_nop 0
	v_add_f32_e32 v13, v10, v11
	v_fmac_f32_e32 v39, 0xba800000, v13
	v_fmac_f32_e32 v38, 0xba800000, v13
	v_fmac_f32_e32 v41, 0xba800000, v13
	v_fmac_f32_e32 v40, 0xba800000, v13
	v_mul_f32_e32 v10, v38, v38
	v_mul_f32_e32 v11, v39, v39
	v_fmac_f32_e32 v10, v40, v40
	v_fmac_f32_e32 v11, v41, v41
	v_fmac_f32_e32 v9, 0xba800000, v13
	v_fmac_f32_e32 v8, 0xba800000, v13
	v_add_f32_e32 v10, v10, v11
	v_fmac_f32_e32 v37, 0xba800000, v13
	v_fmac_f32_e32 v36, 0xba800000, v13
	v_mul_f32_e32 v11, v8, v8
	v_mul_f32_e32 v15, v9, v9
	v_fmac_f32_e32 v11, v36, v36
	v_fmac_f32_e32 v15, v37, v37
	v_add_f32_e32 v11, v11, v15
	v_fmac_f32_e32 v35, 0xba800000, v13
	v_fmac_f32_e32 v33, 0xba800000, v13
	v_add_f32_e32 v10, v10, v11
	v_fmac_f32_e32 v34, 0xba800000, v13
	v_fmac_f32_e32 v32, 0xba800000, v13
	v_mul_f32_e32 v11, v33, v33
	v_mul_f32_e32 v15, v35, v35
	v_fmac_f32_e32 v11, v32, v32
	v_fmac_f32_e32 v15, v34, v34
	v_add_f32_e32 v11, v11, v15
	v_fmac_f32_e32 v26, 0xba800000, v13
	v_fmac_f32_e32 v42, 0xba800000, v13
	v_add_f32_e32 v10, v11, v10
	v_fmac_f32_e32 v14, 0xba800000, v13
	v_fmac_f32_e32 v12, 0xba800000, v13
	v_mul_f32_e32 v11, v42, v42
	v_mul_f32_e32 v15, v26, v26
	v_fmac_f32_e32 v11, v12, v12
	v_fmac_f32_e32 v15, v14, v14
	v_add_f32_e32 v11, v11, v15
	v_add_f32_e32 v10, v11, v10
	s_nop 1
	v_add_f32_dpp v10, v10, v10 quad_perm:[1,0,3,2] row_mask:0xf bank_mask:0xf bound_ctrl:1
	s_nop 1
	v_add_f32_dpp v10, v10, v10 quad_perm:[2,3,0,1] row_mask:0xf bank_mask:0xf bound_ctrl:1
	s_nop 1
	v_add_f32_dpp v10, v10, v10 row_half_mirror row_mask:0xf bank_mask:0xf bound_ctrl:1
	s_nop 1
	v_add_f32_dpp v10, v10, v10 row_mirror row_mask:0xf bank_mask:0xf bound_ctrl:1
	s_nop 0
	v_readlane_b32 s5, v10, 16
	v_readlane_b32 s4, v10, 0
	s_nop 0
	v_mov_b32_e32 v11, s5
	v_readlane_b32 s5, v10, 48
	v_add_f32_e32 v11, s4, v11
	v_readlane_b32 s4, v10, 32
	v_mov_b32_e32 v10, s5
	s_nop 0
	v_add_f32_e32 v10, s4, v10
	v_add_f32_e32 v10, v11, v10
	v_fmamk_f32 v10, v10, 0x3a800000, v201
	s_mov_b32 s4, 0xf800000
	v_mul_f32_e32 v11, 0x4f800000, v10
	v_cmp_gt_f32_e32 vcc, s4, v10
	s_nop 1
	v_cndmask_b32_e32 v10, v10, v11, vcc
	v_sqrt_f32_e32 v11, v10
	s_nop 0
	v_add_u32_e32 v15, -1, v11
	v_fma_f32 v17, -v15, v11, v10
	v_cmp_ge_f32_e64 s[12:13], 0, v17
	v_add_u32_e32 v17, 1, v11
	s_nop 0
	v_cndmask_b32_e64 v15, v11, v15, s[12:13]
	v_fma_f32 v11, -v17, v11, v10
	v_cmp_lt_f32_e64 s[12:13], 0, v11
	s_nop 1
	v_cndmask_b32_e64 v11, v15, v17, s[12:13]
	v_mul_f32_e32 v15, 0x37800000, v11
	v_cndmask_b32_e32 v11, v11, v15, vcc
	v_cmp_class_f32_e32 vcc, v10, v202
	v_mov_b32_e32 v15, 0
	s_nop 0
	v_cndmask_b32_e32 v10, v11, v10, vcc
	v_div_scale_f32 v11, s[4:5], v10, v10, 1.0
	v_rcp_f32_e32 v17, v11
	s_nop 0
	v_fma_f32 v25, -v11, v17, 1.0
	v_fmac_f32_e32 v17, v25, v17
	v_div_scale_f32 v25, vcc, 1.0, v10, 1.0
	v_mul_f32_e32 v27, v25, v17
	v_fma_f32 v43, -v11, v27, v25
	v_fmac_f32_e32 v27, v43, v17
	v_fma_f32 v11, -v11, v27, v25
	v_div_fmas_f32 v11, v11, v17, v27
	s_and_saveexec_b64 s[4:5], s[10:11]
	s_xor_b64 s[4:5], exec, s[4:5]
	s_ashr_i32 s7, s6, 31
	s_or_saveexec_b64 s[4:5], s[4:5]
	v_div_fixup_f32 v44, v11, v10, 1.0
	v_mov_b64_e32 v[10:11], s[6:7]
	s_xor_b64 exec, exec, s[4:5]
	s_cbranch_execz .LBB0_415
	s_ashr_i32 s7, s6, 31
	s_lshl_b64 s[12:13], s[6:7], 3
	s_add_u32 s12, s39, s12
	v_mul_f32_e32 v10, 0x3a800000, v13
	s_addc_u32 s13, s0, s13
	v_mov_b32_e32 v11, v44
	global_store_dwordx2 v24, v[10:11], s[12:13]
	v_mov_b64_e32 v[10:11], s[6:7]
	s_branch .LBB0_415
